# v53 + T5: fp8 expert-output rows (read once) loaded with the nt hint
# baseline (speedup 1.0000x reference)
.LBB0_1533:
	s_add_u32 s2, s10, 0x1fc00000
	s_addc_u32 s3, s11, 0
	s_add_u32 s12, s10, 0x39c00000
	s_addc_u32 s13, s11, 0
	s_ashr_i32 s9, s8, 31
	s_sub_i32 s15, s8, s86
	s_lshl_b64 s[16:17], s[8:9], 12
	s_add_u32 s16, s2, s16
	v_lshlrev_b32_e32 v128, 3, v14
	s_waitcnt vmcnt(2)
	v_readlane_b32 s72, v64, s15
	s_addc_u32 s17, s3, s17
	v_lshl_add_u64 v[8:9], s[2:3], 0, v[128:129]
	s_lshl_b64 s[2:3], s[72:73], 11
	v_readlane_b32 s14, v55, s15
	s_add_u32 s2, s12, s2
	s_mov_b32 s15, s73
	v_lshl_add_u64 v[2:3], s[10:11], 0, v[128:129]
	s_addc_u32 s3, s13, s3
	s_lshl_b64 s[10:11], s[14:15], 11
	global_load_dwordx2 v[0:1], v128, s[16:17]
	global_load_dwordx2 v[4:5], v128, s[16:17] offset:512
	global_load_dwordx2 v[12:13], v128, s[16:17] offset:1024
	global_load_dwordx2 v[16:17], v128, s[16:17] offset:1536
	global_load_dwordx2 v[18:19], v128, s[16:17] offset:2048
	global_load_dwordx2 v[20:21], v128, s[16:17] offset:2560
	global_load_dwordx2 v[22:23], v128, s[16:17] offset:3072
	global_load_dwordx2 v[24:25], v128, s[16:17] offset:3584
	v_lshlrev_b32_e32 v128, 2, v14
	s_add_u32 s10, s12, s10
	s_addc_u32 s11, s13, s11
	global_load_dword v83, v128, s[2:3] offset:1792 nt
	global_load_dword v79, v128, s[2:3] offset:1536 nt
	global_load_dword v77, v128, s[2:3] offset:1280 nt
	global_load_dword v76, v128, s[2:3] offset:1024 nt
	global_load_dword v74, v128, s[2:3] offset:768 nt
	global_load_dword v72, v128, s[2:3] offset:512 nt
	global_load_dword v71, v128, s[2:3] offset:256 nt
	global_load_dword v69, v128, s[2:3] nt
	global_load_dword v82, v128, s[10:11] offset:1792 nt
	global_load_dword v81, v128, s[10:11] offset:1536 nt
	global_load_dword v80, v128, s[10:11] offset:1280 nt
	global_load_dword v78, v128, s[10:11] offset:1024 nt
	global_load_dword v75, v128, s[10:11] offset:768 nt
	global_load_dword v73, v128, s[10:11] offset:512 nt
	global_load_dword v70, v128, s[10:11] offset:256 nt
	global_load_dword v68, v128, s[10:11] nt
	s_mov_b64 s[2:3], 0x28c00000
	v_lshl_add_u64 v[10:11], v[2:3], 0, s[2:3]
	v_lshl_add_u32 v67, v14, 4, 0
	v_readlane_b32 s9, v254, 23
	s_waitcnt vmcnt(22)
	v_lshlrev_b32_e32 v6, 16, v4
	v_and_b32_e32 v7, 0xffff0000, v4
	v_lshlrev_b32_e32 v4, 16, v5
	v_and_b32_e32 v5, 0xffff0000, v5
	s_waitcnt vmcnt(21)
	v_lshlrev_b32_e32 v32, 16, v12
	v_lshlrev_b32_e32 v2, 16, v0
	v_and_b32_e32 v3, 0xffff0000, v0
	v_lshlrev_b32_e32 v0, 16, v1
	v_and_b32_e32 v1, 0xffff0000, v1
	v_and_b32_e32 v33, 0xffff0000, v12
	v_lshlrev_b32_e32 v30, 16, v13
	v_and_b32_e32 v31, 0xffff0000, v13
	s_waitcnt vmcnt(20)
	v_lshlrev_b32_e32 v40, 16, v16
	v_and_b32_e32 v41, 0xffff0000, v16
	v_lshlrev_b32_e32 v38, 16, v17
	v_and_b32_e32 v39, 0xffff0000, v17
	s_waitcnt vmcnt(19)
	v_lshlrev_b32_e32 v36, 16, v18
	v_and_b32_e32 v37, 0xffff0000, v18
	v_lshlrev_b32_e32 v34, 16, v19
	v_and_b32_e32 v35, 0xffff0000, v19
	s_waitcnt vmcnt(18)
	v_lshlrev_b32_e32 v52, 16, v20
	v_and_b32_e32 v53, 0xffff0000, v20
	v_lshlrev_b32_e32 v50, 16, v21
	v_and_b32_e32 v51, 0xffff0000, v21
	s_waitcnt vmcnt(17)
	v_lshlrev_b32_e32 v48, 16, v22
	v_and_b32_e32 v49, 0xffff0000, v22
	v_lshlrev_b32_e32 v46, 16, v23
	v_and_b32_e32 v47, 0xffff0000, v23
	s_waitcnt vmcnt(16)
	v_lshlrev_b32_e32 v42, 16, v24
	v_and_b32_e32 v43, 0xffff0000, v24
	v_lshlrev_b32_e32 v44, 16, v25
	v_and_b32_e32 v45, 0xffff0000, v25
	v_lshl_add_u64 v[12:13], s[12:13], 0, v[128:129]
	v_lshlrev_b32_e32 v128, 4, v14
	s_branch .LBB0_1535

.LBB0_1536:
	s_add_i32 s8, s8, 1
	s_cmp_lt_i32 s8, s55
	s_cselect_b64 s[12:13], -1, 0
	s_cmp_ge_i32 s8, s55
	s_mul_hi_i32 s2, s8, 0x38e38e39
	s_cselect_b64 s[10:11], -1, 0
	s_lshr_b32 s3, s2, 31
	s_ashr_i32 s2, s2, 9
	s_add_i32 s2, s2, s3
	s_mulk_i32 s2, 0x900
	s_sub_i32 s2, s8, s2
	s_cmpk_lt_i32 s2, 0x100
	s_cselect_b64 s[2:3], -1, 0
	s_and_b64 s[2:3], s[0:1], s[2:3]
	s_and_b64 s[2:3], s[12:13], s[2:3]
	s_and_b64 vcc, exec, s[2:3]
	s_cbranch_vccnz .LBB0_1536
	s_and_b64 s[2:3], s[12:13], exec
	s_cselect_b32 s2, s8, s16
	s_sub_i32 s3, s2, s86
	v_readlane_b32 s72, v55, s3
	v_readlane_b32 s12, v64, s3
	s_ashr_i32 s3, s2, 31
	s_lshl_b64 s[2:3], s[2:3], 12
	v_lshl_add_u64 v[14:15], v[8:9], 0, s[2:3]
	s_lshl_b64 s[2:3], s[72:73], 11
	s_mov_b32 s13, s73
	v_lshl_add_u64 v[82:83], v[12:13], 0, s[2:3]
	s_mul_hi_i32 s2, s16, 0x38e38e39
	s_lshl_b64 s[12:13], s[12:13], 11
	s_lshr_b32 s3, s2, 31
	s_ashr_i32 s2, s2, 9
	v_lshl_add_u64 v[92:93], v[12:13], 0, s[12:13]
	s_add_i32 s12, s2, s3
	s_mul_i32 s2, s12, 0x900
	s_sub_i32 s14, s16, s2
	global_load_dwordx2 v[28:29], v[14:15], off
	global_load_dwordx2 v[26:27], v[14:15], off offset:512
	global_load_dwordx2 v[24:25], v[14:15], off offset:1024
	global_load_dwordx2 v[22:23], v[14:15], off offset:1536
	global_load_dwordx2 v[20:21], v[14:15], off offset:2048
	global_load_dwordx2 v[18:19], v[14:15], off offset:2560
	global_load_dwordx2 v[16:17], v[14:15], off offset:3072
	s_nop 0
	global_load_dwordx2 v[14:15], v[14:15], off offset:3584
	s_cmpk_gt_i32 s14, 0xff
	global_load_dword v68, v[82:83], off nt
	global_load_dword v69, v[92:93], off nt
	global_load_dword v70, v[82:83], off offset:256 nt
	global_load_dword v71, v[92:93], off offset:256 nt
	global_load_dword v73, v[82:83], off offset:512 nt
	global_load_dword v72, v[92:93], off offset:512 nt
	global_load_dword v75, v[82:83], off offset:768 nt
	global_load_dword v74, v[92:93], off offset:768 nt
	global_load_dword v78, v[82:83], off offset:1024 nt
	global_load_dword v76, v[92:93], off offset:1024 nt
	global_load_dword v80, v[82:83], off offset:1280 nt
	global_load_dword v77, v[92:93], off offset:1280 nt
	global_load_dword v81, v[82:83], off offset:1536 nt
	global_load_dword v79, v[92:93], off offset:1536 nt
	s_nop 0
	global_load_dword v82, v[82:83], off offset:1792 nt
	s_nop 0
	global_load_dword v83, v[92:93], off offset:1792 nt
	s_cselect_b32 s2, s12, 8
	v_cvt_pk_f32_fp8_e32 v[92:93], v91
	v_cvt_pk_f32_fp8_sdwa v[94:95], v91 src0_sel:WORD_1
	v_cvt_pk_f32_fp8_e32 v[96:97], v90
	v_cvt_pk_f32_fp8_sdwa v[90:91], v90 src0_sel:WORD_1
	s_cmp_eq_u32 s2, s9
	s_cselect_b32 s2, 0, 0x6000
	s_sub_i32 s3, s16, s86
	v_readlane_b32 s20, v65, s3
	v_readlane_b32 s18, v66, s3
	v_add_u32_e32 v84, s2, v67
	v_pk_mul_f32 v[90:91], v[90:91], s[20:21] op_sel_hi:[1,0]
	v_pk_mul_f32 v[96:97], v[96:97], s[20:21] op_sel_hi:[1,0]
	v_pk_fma_f32 v[94:95], v[94:95], s[18:19], v[90:91] op_sel_hi:[1,0,1]
	v_pk_fma_f32 v[96:97], v[92:93], s[18:19], v[96:97] op_sel_hi:[1,0,1]
	ds_read_b128 v[90:93], v84
	s_mov_b32 s2, 0x800000
	s_waitcnt lgkmcnt(0)
	v_pk_fma_f32 v[0:1], v[92:93], v[94:95], v[0:1]
	v_pk_fma_f32 v[2:3], v[90:91], v[96:97], v[2:3]
	v_cvt_pk_f32_fp8_e32 v[90:91], v89
	v_cvt_pk_f32_fp8_sdwa v[92:93], v89 src0_sel:WORD_1
	v_cvt_pk_f32_fp8_e32 v[94:95], v88
	v_cvt_pk_f32_fp8_sdwa v[88:89], v88 src0_sel:WORD_1
	v_pk_mul_f32 v[94:95], v[94:95], s[20:21] op_sel_hi:[1,0]
	v_pk_mul_f32 v[88:89], v[88:89], s[20:21] op_sel_hi:[1,0]
	v_pk_fma_f32 v[94:95], v[90:91], s[18:19], v[94:95] op_sel_hi:[1,0,1]
	v_pk_fma_f32 v[92:93], v[92:93], s[18:19], v[88:89] op_sel_hi:[1,0,1]
	ds_read_b128 v[88:91], v84 offset:1024
	s_waitcnt lgkmcnt(0)
	v_pk_fma_f32 v[4:5], v[90:91], v[92:93], v[4:5]
	v_pk_fma_f32 v[6:7], v[88:89], v[94:95], v[6:7]
	v_cvt_pk_f32_fp8_e32 v[88:89], v87
	v_cvt_pk_f32_fp8_sdwa v[90:91], v87 src0_sel:WORD_1
	v_cvt_pk_f32_fp8_e32 v[92:93], v86
	v_cvt_pk_f32_fp8_sdwa v[86:87], v86 src0_sel:WORD_1
	v_pk_mul_f32 v[92:93], v[92:93], s[20:21] op_sel_hi:[1,0]
	v_pk_mul_f32 v[86:87], v[86:87], s[20:21] op_sel_hi:[1,0]
	v_pk_fma_f32 v[92:93], v[88:89], s[18:19], v[92:93] op_sel_hi:[1,0,1]
	v_pk_fma_f32 v[90:91], v[90:91], s[18:19], v[86:87] op_sel_hi:[1,0,1]
	ds_read_b128 v[86:89], v84 offset:2048
	s_waitcnt lgkmcnt(0)
	v_pk_fma_f32 v[30:31], v[88:89], v[90:91], v[30:31]
	v_pk_fma_f32 v[32:33], v[86:87], v[92:93], v[32:33]
	v_cvt_pk_f32_fp8_e32 v[90:91], v63
	v_cvt_pk_f32_fp8_sdwa v[92:93], v63 src0_sel:WORD_1
	v_cvt_pk_f32_fp8_e32 v[86:87], v85
	v_cvt_pk_f32_fp8_sdwa v[88:89], v85 src0_sel:WORD_1
	v_pk_mul_f32 v[90:91], v[90:91], s[20:21] op_sel_hi:[1,0]
	v_pk_mul_f32 v[92:93], v[92:93], s[20:21] op_sel_hi:[1,0]
	v_pk_fma_f32 v[90:91], v[86:87], s[18:19], v[90:91] op_sel_hi:[1,0,1]
	v_pk_fma_f32 v[92:93], v[88:89], s[18:19], v[92:93] op_sel_hi:[1,0,1]
	ds_read_b128 v[86:89], v84 offset:3072
	s_waitcnt lgkmcnt(0)
	v_pk_fma_f32 v[38:39], v[88:89], v[92:93], v[38:39]
	v_cvt_pk_f32_fp8_e32 v[88:89], v61
	v_pk_fma_f32 v[40:41], v[86:87], v[90:91], v[40:41]
	v_cvt_pk_f32_fp8_e32 v[86:87], v62
	v_cvt_pk_f32_fp8_sdwa v[90:91], v61 src0_sel:WORD_1
	v_pk_mul_f32 v[88:89], v[88:89], s[20:21] op_sel_hi:[1,0]
	v_cvt_pk_f32_fp8_sdwa v[62:63], v62 src0_sel:WORD_1
	v_pk_fma_f32 v[92:93], v[86:87], s[18:19], v[88:89] op_sel_hi:[1,0,1]
	ds_read_b128 v[86:89], v84 offset:4096
	v_pk_mul_f32 v[90:91], v[90:91], s[20:21] op_sel_hi:[1,0]
	s_waitcnt lgkmcnt(0)
	v_pk_fma_f32 v[36:37], v[86:87], v[92:93], v[36:37]
	v_pk_fma_f32 v[62:63], v[62:63], s[18:19], v[90:91] op_sel_hi:[1,0,1]
	v_cvt_pk_f32_fp8_e32 v[86:87], v59
	v_pk_fma_f32 v[34:35], v[88:89], v[62:63], v[34:35]
	v_cvt_pk_f32_fp8_sdwa v[88:89], v59 src0_sel:WORD_1
	v_cvt_pk_f32_fp8_e32 v[62:63], v60
	v_cvt_pk_f32_fp8_sdwa v[60:61], v60 src0_sel:WORD_1
	v_pk_mul_f32 v[86:87], v[86:87], s[20:21] op_sel_hi:[1,0]
	v_pk_mul_f32 v[88:89], v[88:89], s[20:21] op_sel_hi:[1,0]
	v_pk_fma_f32 v[86:87], v[62:63], s[18:19], v[86:87] op_sel_hi:[1,0,1]
	v_pk_fma_f32 v[88:89], v[60:61], s[18:19], v[88:89] op_sel_hi:[1,0,1]
	ds_read_b128 v[60:63], v84 offset:5120
	s_waitcnt lgkmcnt(0)
	v_pk_fma_f32 v[50:51], v[62:63], v[88:89], v[50:51]
	v_pk_fma_f32 v[52:53], v[60:61], v[86:87], v[52:53]
	v_cvt_pk_f32_fp8_e32 v[62:63], v57
	v_cvt_pk_f32_fp8_sdwa v[86:87], v57 src0_sel:WORD_1
	v_cvt_pk_f32_fp8_e32 v[60:61], v58
	v_cvt_pk_f32_fp8_sdwa v[58:59], v58 src0_sel:WORD_1
	v_pk_mul_f32 v[62:63], v[62:63], s[20:21] op_sel_hi:[1,0]
	v_pk_mul_f32 v[86:87], v[86:87], s[20:21] op_sel_hi:[1,0]
	v_pk_fma_f32 v[62:63], v[60:61], s[18:19], v[62:63] op_sel_hi:[1,0,1]
	v_pk_fma_f32 v[86:87], v[58:59], s[18:19], v[86:87] op_sel_hi:[1,0,1]
	ds_read_b128 v[58:61], v84 offset:6144
	s_waitcnt lgkmcnt(0)
	v_pk_fma_f32 v[46:47], v[60:61], v[86:87], v[46:47]
	v_pk_fma_f32 v[48:49], v[58:59], v[62:63], v[48:49]
	v_cvt_pk_f32_fp8_e32 v[60:61], v54
	v_cvt_pk_f32_fp8_sdwa v[62:63], v54 src0_sel:WORD_1
	v_cvt_pk_f32_fp8_e32 v[58:59], v56
	v_cvt_pk_f32_fp8_sdwa v[56:57], v56 src0_sel:WORD_1
	v_pk_mul_f32 v[60:61], v[60:61], s[20:21] op_sel_hi:[1,0]
	v_pk_mul_f32 v[62:63], v[62:63], s[20:21] op_sel_hi:[1,0]
	v_pk_fma_f32 v[60:61], v[58:59], s[18:19], v[60:61] op_sel_hi:[1,0,1]
	v_pk_fma_f32 v[62:63], v[56:57], s[18:19], v[62:63] op_sel_hi:[1,0,1]
	ds_read_b128 v[56:59], v84 offset:7168
	v_mul_f32_e32 v54, v3, v3
	v_fmac_f32_e32 v54, v2, v2
	s_mov_b64 s[18:19], -1
	s_waitcnt lgkmcnt(0)
	v_pk_fma_f32 v[42:43], v[56:57], v[60:61], v[42:43]
	v_mul_f32_e32 v56, v1, v1
	v_fmac_f32_e32 v56, v0, v0
	v_add_f32_e32 v54, v54, v56
	v_mul_f32_e32 v56, v7, v7
	v_mul_f32_e32 v57, v5, v5
	v_fmac_f32_e32 v56, v6, v6
	v_fmac_f32_e32 v57, v4, v4
	v_add_f32_e32 v56, v56, v57
	v_add_f32_e32 v54, v54, v56
	v_mul_f32_e32 v56, v33, v33
	v_mul_f32_e32 v57, v31, v31
	v_fmac_f32_e32 v56, v32, v32
	v_fmac_f32_e32 v57, v30, v30
	v_add_f32_e32 v56, v56, v57
	v_add_f32_e32 v54, v56, v54
	v_mul_f32_e32 v56, v41, v41
	v_mul_f32_e32 v57, v39, v39
	v_fmac_f32_e32 v56, v40, v40
	v_fmac_f32_e32 v57, v38, v38
	v_add_f32_e32 v56, v56, v57
	v_add_f32_e32 v54, v56, v54
	v_mul_f32_e32 v56, v37, v37
	v_mul_f32_e32 v57, v35, v35
	v_fmac_f32_e32 v56, v36, v36
	v_fmac_f32_e32 v57, v34, v34
	v_add_f32_e32 v56, v56, v57
	v_add_f32_e32 v54, v56, v54
	v_mul_f32_e32 v56, v53, v53
	v_mul_f32_e32 v57, v51, v51
	v_fmac_f32_e32 v56, v52, v52
	v_fmac_f32_e32 v57, v50, v50
	v_add_f32_e32 v56, v56, v57
	v_add_f32_e32 v54, v56, v54
	v_mul_f32_e32 v56, v49, v49
	v_mul_f32_e32 v57, v47, v47
	v_fmac_f32_e32 v56, v48, v48
	v_fmac_f32_e32 v57, v46, v46
	v_pk_fma_f32 v[44:45], v[58:59], v[62:63], v[44:45]
	v_add_f32_e32 v56, v56, v57
	v_add_f32_e32 v54, v56, v54
	v_mul_f32_e32 v56, v43, v43
	v_mul_f32_e32 v57, v45, v45
	v_fmac_f32_e32 v56, v42, v42
	v_fmac_f32_e32 v57, v44, v44
	v_add_f32_e32 v56, v56, v57
	v_add_f32_e32 v54, v56, v54
	s_nop 1
	v_add_f32_dpp v54, v54, v54 quad_perm:[1,0,3,2] row_mask:0xf bank_mask:0xf bound_ctrl:1
	s_nop 1
	v_add_f32_dpp v54, v54, v54 quad_perm:[2,3,0,1] row_mask:0xf bank_mask:0xf bound_ctrl:1
	s_nop 1
	v_add_f32_dpp v54, v54, v54 row_half_mirror row_mask:0xf bank_mask:0xf bound_ctrl:1
	s_nop 1
	v_add_f32_dpp v54, v54, v54 row_mirror row_mask:0xf bank_mask:0xf bound_ctrl:1
	v_mov_b32_e32 v56, v54
	s_nop 1
	v_permlane16_swap_b32_e32 v54, v56
	v_add_f32_e32 v54, v54, v56
	v_mov_b32_e32 v56, v54
	s_nop 1
	v_permlane32_swap_b32_e32 v54, v56
	v_add_f32_e32 v54, v54, v56
	v_fmamk_f32 v54, v54, 0x3a000000, v248
	v_cmp_gt_f32_e32 vcc, s2, v54
	v_mul_f32_e32 v56, 0x4b800000, v54
	s_nop 0
	v_cndmask_b32_e32 v54, v54, v56, vcc
	v_rsq_f32_e32 v54, v54
	s_nop 0
	v_mul_f32_e32 v56, 0x45800000, v54
	v_cndmask_b32_e32 v54, v54, v56, vcc
	s_and_b64 vcc, exec, s[24:25]
	s_cbranch_vccz .LBB0_1539
	s_ashr_i32 s17, s16, 31
	s_lshl_b64 s[16:17], s[16:17], 12
	v_cvt_pk_bf16_f32 v56, v2, v3
	v_cvt_pk_bf16_f32 v57, v0, v1
	v_lshl_add_u64 v[58:59], v[8:9], 0, s[16:17]
	global_store_dwordx2 v[58:59], v[56:57], off
	v_cvt_pk_bf16_f32 v56, v6, v7
	v_cvt_pk_bf16_f32 v57, v4, v5
	global_store_dwordx2 v[58:59], v[56:57], off offset:512
	v_cvt_pk_bf16_f32 v56, v32, v33
	v_cvt_pk_bf16_f32 v57, v30, v31
	global_store_dwordx2 v[58:59], v[56:57], off offset:1024
	v_cvt_pk_bf16_f32 v56, v40, v41
	v_cvt_pk_bf16_f32 v57, v38, v39
	global_store_dwordx2 v[58:59], v[56:57], off offset:1536
	v_cvt_pk_bf16_f32 v56, v36, v37
	v_cvt_pk_bf16_f32 v57, v34, v35
	global_store_dwordx2 v[58:59], v[56:57], off offset:2048
	v_cvt_pk_bf16_f32 v56, v52, v53
	v_cvt_pk_bf16_f32 v57, v50, v51
	global_store_dwordx2 v[58:59], v[56:57], off offset:2560
	v_cvt_pk_bf16_f32 v56, v48, v49
	v_cvt_pk_bf16_f32 v57, v46, v47
	global_store_dwordx2 v[58:59], v[56:57], off offset:3072
	v_cvt_pk_bf16_f32 v56, v42, v43
	v_cvt_pk_bf16_f32 v57, v44, v45
	global_store_dwordx2 v[58:59], v[56:57], off offset:3584
	ds_read_b128 v[58:61], v84 offset:8192
	ds_read_b128 v[86:89], v84 offset:16384
	v_pk_mul_f32 v[56:57], v[54:55], v[0:1] op_sel_hi:[0,1]
	v_pk_mul_f32 v[62:63], v[54:55], v[2:3] op_sel_hi:[0,1]
	v_pk_mul_f32 v[94:95], v[54:55], v[30:31] op_sel_hi:[0,1]
	v_pk_mul_f32 v[96:97], v[54:55], v[32:33] op_sel_hi:[0,1]
	s_waitcnt lgkmcnt(0)
	v_pk_fma_f32 v[56:57], v[56:57], v[60:61], v[88:89]
	v_pk_fma_f32 v[58:59], v[62:63], v[58:59], v[86:87]
	ds_read_b128 v[86:89], v84 offset:9216
	ds_read_b128 v[90:93], v84 offset:17408
	v_pk_mul_f32 v[60:61], v[54:55], v[4:5] op_sel_hi:[0,1]
	v_pk_mul_f32 v[62:63], v[54:55], v[6:7] op_sel_hi:[0,1]
	v_pk_mul_f32 v[98:99], v[54:55], v[38:39] op_sel_hi:[0,1]
	v_pk_mul_f32 v[100:101], v[54:55], v[40:41] op_sel_hi:[0,1]
	s_waitcnt lgkmcnt(0)
	v_pk_fma_f32 v[60:61], v[60:61], v[88:89], v[92:93]
	v_pk_fma_f32 v[62:63], v[62:63], v[86:87], v[90:91]
	ds_read_b128 v[86:89], v84 offset:10240
	ds_read_b128 v[90:93], v84 offset:18432
	v_pk_mul_f32 v[102:103], v[54:55], v[34:35] op_sel_hi:[0,1]
	v_pk_mul_f32 v[104:105], v[54:55], v[36:37] op_sel_hi:[0,1]
	v_pk_mul_f32 v[106:107], v[54:55], v[50:51] op_sel_hi:[0,1]
	v_pk_mul_f32 v[108:109], v[54:55], v[52:53] op_sel_hi:[0,1]
	s_waitcnt lgkmcnt(0)
	v_pk_fma_f32 v[94:95], v[94:95], v[88:89], v[92:93]
	v_pk_fma_f32 v[96:97], v[96:97], v[86:87], v[90:91]
	ds_read_b128 v[86:89], v84 offset:11264
	ds_read_b128 v[90:93], v84 offset:19456
	v_pk_mul_f32 v[110:111], v[54:55], v[46:47] op_sel_hi:[0,1]
	v_pk_mul_f32 v[112:113], v[54:55], v[48:49] op_sel_hi:[0,1]
	v_pk_mul_f32 v[114:115], v[54:55], v[44:45] op_sel_hi:[0,1]
	v_pk_mul_f32 v[116:117], v[54:55], v[42:43] op_sel_hi:[0,1]
	s_waitcnt lgkmcnt(0)
	v_pk_fma_f32 v[98:99], v[98:99], v[88:89], v[92:93]
	v_pk_fma_f32 v[100:101], v[100:101], v[86:87], v[90:91]
	ds_read_b128 v[86:89], v84 offset:12288
	ds_read_b128 v[90:93], v84 offset:20480
	s_mov_b64 s[18:19], 0
	s_waitcnt lgkmcnt(0)
	v_pk_fma_f32 v[102:103], v[102:103], v[88:89], v[92:93]
	v_pk_fma_f32 v[104:105], v[104:105], v[86:87], v[90:91]
	ds_read_b128 v[86:89], v84 offset:13312
	ds_read_b128 v[90:93], v84 offset:21504
	s_waitcnt lgkmcnt(0)
	v_pk_fma_f32 v[106:107], v[106:107], v[88:89], v[92:93]
	v_pk_fma_f32 v[108:109], v[108:109], v[86:87], v[90:91]
	ds_read_b128 v[86:89], v84 offset:14336
	ds_read_b128 v[90:93], v84 offset:22528
	s_waitcnt lgkmcnt(0)
	v_pk_fma_f32 v[110:111], v[110:111], v[88:89], v[92:93]
	v_pk_fma_f32 v[112:113], v[112:113], v[86:87], v[90:91]
	ds_read_b128 v[86:89], v84 offset:15360
	ds_read_b128 v[90:93], v84 offset:23552
	v_cvt_pk_bf16_f32 v58, v58, v59
	v_cvt_pk_bf16_f32 v59, v56, v57
	v_lshl_add_u64 v[56:57], v[10:11], 0, s[16:17]
	global_store_dwordx2 v[56:57], v[58:59], off
	v_cvt_pk_bf16_f32 v58, v62, v63
	v_cvt_pk_bf16_f32 v59, v60, v61
	global_store_dwordx2 v[56:57], v[58:59], off offset:512
	v_cvt_pk_bf16_f32 v58, v96, v97
	v_cvt_pk_bf16_f32 v59, v94, v95
	global_store_dwordx2 v[56:57], v[58:59], off offset:1024
	v_cvt_pk_bf16_f32 v58, v100, v101
	v_cvt_pk_bf16_f32 v59, v98, v99
	global_store_dwordx2 v[56:57], v[58:59], off offset:1536
	v_cvt_pk_bf16_f32 v58, v104, v105
	v_cvt_pk_bf16_f32 v59, v102, v103
	global_store_dwordx2 v[56:57], v[58:59], off offset:2048
	v_cvt_pk_bf16_f32 v58, v108, v109
	v_cvt_pk_bf16_f32 v59, v106, v107
	global_store_dwordx2 v[56:57], v[58:59], off offset:2560
	v_cvt_pk_bf16_f32 v58, v112, v113
	v_cvt_pk_bf16_f32 v59, v110, v111
	s_waitcnt lgkmcnt(0)
	v_pk_fma_f32 v[88:89], v[114:115], v[88:89], v[92:93]
	v_pk_fma_f32 v[86:87], v[116:117], v[86:87], v[90:91]
	global_store_dwordx2 v[56:57], v[58:59], off offset:3072
	v_cvt_pk_bf16_f32 v58, v86, v87
	v_cvt_pk_bf16_f32 v59, v88, v89
	global_store_dwordx2 v[56:57], v[58:59], off offset:3584
